# NSA tile loop: PV(it-1)+branch-end RMW moved from the DMA/QK segment to the end of the softmax segment (segment balance)
# baseline (speedup 1.0000x reference)
; #define LAS __attribute__((address_space(3)))
; __device__ __forceinline__ void nsa_pv_rd4(const LAS unsigned char* vA, int sv, int step, bf16x8 (&af)[4]) {
; #pragma unroll
;     for (int dt = 0; dt < 4; ++dt) af[dt] = *(const LAS bf16x8*)(vA + dt * 4096 + (((2 * step) * 16) ^ sv));
; }
; __device__ __forceinline__ void nsa_pv_mm4(const bf16x8 (&af)[4], const bf16x8& pfk, f32x16 (&o)[4]) {
; #pragma unroll
;     for (int dt = 0; dt < 4; ++dt) o[dt] = __builtin_amdgcn_mfma_f32_32x32x16_bf16(af[dt], pfk, o[dt], 0, 0, 0);
; }
; __device__ __forceinline__ void nsa_pv_sw(const LAS unsigned char* vbuf, const bf16x8 (&pf)[2][2], f32x16 (&o)[4], int r, int h) {
;     const int sv = (((r >> 1) & 7) ^ h) * 16; const LAS unsigned char* vA = vbuf + r * 128;
; #pragma unroll
;     for (int step = 0; step < 4; ++step) { bf16x8 fa[4];
;         nsa_pv_rd4(vA, sv, step, fa); __builtin_amdgcn_sched_barrier(0);
;         nsa_pv_mm4(fa, pf[step >> 1][step & 1], o); __builtin_amdgcn_sched_barrier(0); }
; __device__ __forceinline__ void nsa_unit(const Args& a, LAS unsigned char* lds, int b, int kvh, int qb) {
;     ...
;             const float nmc = lane_on ? -mrun * SM_C : NINF;
;             float ls = 0.f;
; #pragma unroll
;             for (int i = 0; i < 16; ++i) { p0[i] = __builtin_amdgcn_exp2f(fmaf(p0[i], SM_C, nmc)); p1[i] = __builtin_amdgcn_exp2f(fmaf(p1[i], SM_C, nmc)); ls += p0[i] + p1[i]; }
;             lrun = lrun * alpha + ls;
;             pf[0][0] = nsa_pack8(p0, 0); pf[0][1] = nsa_pack8(p0, 1); pf[1][0] = nsa_pack8(p1, 0); pf[1][1] = nsa_pack8(p1, 1);
;         }
;         asm volatile("s_waitcnt lgkmcnt(0)\n\ts_barrier" ::: "memory");
;         if (it + 2 < nTot) { const bf16 *kt, *vt; tile_src(it + 2, kt, vt); const int t2 = it + 2;
;             int lo_ = lane; asm volatile("" : "+v"(lo_)); nsa_dma_tile(kt, PW * 2, vt, VTP * 2, ldsb + (t2 % 3) * NTB, ldsb + VOFF + (t2 & 3) * NTB, w, lo_); }
;         int ro = r, ho = h; asm volatile("" : "+v"(ro), "+v"(ho));
;         if (it > 0) { const int ti = it - 1;
;             nsa_pv_sw(lds + VOFF + (ti & 3) * NTB, pf, o, ro, ho);
;             if (ti == nS - 1 || ti == nTot - 1) {
.LBB0_911:
	v_mul_f32_e32 v34, 0xbe0293ee, v208
	v_cndmask_b32_e64 v190, v244, v34, s[2:3]
	v_fmamk_f32 v34, v78, 0x3e0293ee, v190
	v_exp_f32_e32 v78, v34
	v_fmamk_f32 v34, v62, 0x3e0293ee, v190
	v_exp_f32_e32 v62, v34
	v_fmamk_f32 v34, v79, 0x3e0293ee, v190
	v_fmamk_f32 v36, v80, 0x3e0293ee, v190
	v_exp_f32_e32 v79, v34
	v_fmamk_f32 v34, v63, 0x3e0293ee, v190
	v_exp_f32_e32 v80, v36
	v_fmamk_f32 v36, v64, 0x3e0293ee, v190
	v_exp_f32_e32 v63, v34
	v_exp_f32_e32 v64, v36
	v_fmamk_f32 v36, v81, 0x3e0293ee, v190
	v_exp_f32_e32 v81, v36
	v_fmamk_f32 v36, v65, 0x3e0293ee, v190
	v_exp_f32_e32 v65, v36
	v_add_f32_e32 v34, v78, v62
	v_add_f32_e32 v34, 0, v34
	v_add_f32_e32 v35, v79, v63
	v_add_f32_e32 v34, v35, v34
	v_add_f32_e32 v35, v80, v64
	v_add_f32_e32 v34, v35, v34
	v_add_f32_e32 v35, v81, v65
	v_add_f32_e32 v50, v35, v34
	v_fmamk_f32 v34, v82, 0x3e0293ee, v190
	v_exp_f32_e32 v35, v34
	v_fmamk_f32 v34, v66, 0x3e0293ee, v190
	v_exp_f32_e32 v37, v34
	v_fmamk_f32 v34, v83, 0x3e0293ee, v190
	v_fmamk_f32 v36, v67, 0x3e0293ee, v190
	v_fmamk_f32 v38, v84, 0x3e0293ee, v190
	v_exp_f32_e32 v34, v34
	v_exp_f32_e32 v36, v36
	v_exp_f32_e32 v39, v38
	v_fmamk_f32 v38, v68, 0x3e0293ee, v190
	v_exp_f32_e32 v41, v38
	v_fmamk_f32 v38, v85, 0x3e0293ee, v190
	v_fmamk_f32 v40, v69, 0x3e0293ee, v190
	v_exp_f32_e32 v38, v38
	v_exp_f32_e32 v40, v40
	v_pk_add_f32 v[48:49], v[34:35], v[36:37]
	v_fmamk_f32 v52, v88, 0x3e0293ee, v190
	v_add_f32_e32 v49, v49, v50
	v_add_f32_e32 v50, v48, v49
	v_pk_add_f32 v[48:49], v[38:39], v[40:41]
	v_exp_f32_e32 v53, v52
	v_add_f32_e32 v49, v49, v50
	v_add_f32_e32 v58, v48, v49
	v_fmamk_f32 v48, v86, 0x3e0293ee, v190
	v_exp_f32_e32 v49, v48
	v_fmamk_f32 v48, v70, 0x3e0293ee, v190
	v_exp_f32_e32 v51, v48
	v_fmamk_f32 v48, v87, 0x3e0293ee, v190
	v_fmamk_f32 v50, v71, 0x3e0293ee, v190
	v_exp_f32_e32 v48, v48
	v_exp_f32_e32 v50, v50
	v_fmamk_f32 v52, v72, 0x3e0293ee, v190
	v_exp_f32_e32 v55, v52
	v_fmamk_f32 v52, v89, 0x3e0293ee, v190
	v_fmamk_f32 v54, v73, 0x3e0293ee, v190
	v_exp_f32_e32 v52, v52
	v_exp_f32_e32 v54, v54
	v_pk_add_f32 v[56:57], v[48:49], v[50:51]
	v_fmamk_f32 v60, v92, 0x3e0293ee, v190
	v_add_f32_e32 v57, v57, v58
	v_add_f32_e32 v58, v56, v57
	v_pk_add_f32 v[56:57], v[52:53], v[54:55]
	v_exp_f32_e32 v61, v60
	v_add_f32_e32 v57, v57, v58
	v_add_f32_e32 v68, v56, v57
	v_fmamk_f32 v56, v90, 0x3e0293ee, v190
	v_exp_f32_e32 v57, v56
	v_fmamk_f32 v56, v74, 0x3e0293ee, v190
	v_exp_f32_e32 v59, v56
	v_fmamk_f32 v56, v91, 0x3e0293ee, v190
	v_fmamk_f32 v58, v75, 0x3e0293ee, v190
	v_exp_f32_e32 v56, v56
	v_exp_f32_e32 v58, v58
	v_fmamk_f32 v60, v76, 0x3e0293ee, v190
	v_exp_f32_e32 v211, v60
	v_fmamk_f32 v60, v93, 0x3e0293ee, v190
	v_fmac_f32_e32 v190, 0x3e0293ee, v77
	v_exp_f32_e32 v60, v60
	v_exp_f32_e32 v210, v190
	v_pk_add_f32 v[66:67], v[56:57], v[58:59]
	v_add_f32_e32 v67, v67, v68
	v_add_f32_e32 v66, v66, v67
	v_pk_add_f32 v[190:191], v[60:61], v[210:211]
	v_add_f32_e32 v191, v191, v66
	v_add_f32_e32 v212, v190, v191
	v_fmac_f32_e32 v212, v209, v46
	v_mov_b32_e32 v209, v212
	v_cvt_pk_bf16_f32 v190, v78, v79
	v_cvt_pk_bf16_f32 v191, v80, v81
	v_cvt_pk_bf16_f32 v192, v35, v34
	v_cvt_pk_bf16_f32 v193, v39, v38
	v_cvt_pk_bf16_f32 v194, v49, v48
	v_cvt_pk_bf16_f32 v195, v53, v52
	v_cvt_pk_bf16_f32 v196, v57, v56
	v_cvt_pk_bf16_f32 v197, v61, v60
	v_cvt_pk_bf16_f32 v198, v62, v63
	v_cvt_pk_bf16_f32 v199, v64, v65
	v_cvt_pk_bf16_f32 v200, v37, v36
	v_cvt_pk_bf16_f32 v201, v41, v40
	v_cvt_pk_bf16_f32 v202, v51, v50
	v_cvt_pk_bf16_f32 v203, v55, v54
	v_cvt_pk_bf16_f32 v204, v59, v58
	v_cvt_pk_bf16_f32 v205, v211, v210
	v_mov_b32_e32 v211, v233
	v_mov_b32_e32 v210, v232
	s_and_b32 s0, s75, 0xc000
	v_lshrrev_b32_e32 v34, 1, v210
	s_add_i32 s0, s0, 0
	v_bitop3_b32 v34, v34, v211, 7 bitop3:0x6c
	v_lshlrev_b32_e32 v46, 4, v34
	v_lshl_add_u32 v56, v210, 7, s0
	v_add_u32_e32 v212, v56, v46
	v_xad_u32 v213, v46, 32, v56
	v_xad_u32 v214, v46, 64, v56
	v_xad_u32 v215, v46, s68, v56
	ds_read_b128 v[34:37], v212 offset:49152
	ds_read_b128 v[38:41], v212 offset:53248
	ds_read_b128 v[48:51], v212 offset:57344
	ds_read_b128 v[52:55], v212 offset:61440
	ds_read_b128 v[62:65], v213 offset:49152
	ds_read_b128 v[66:69], v213 offset:53248
	ds_read_b128 v[70:73], v213 offset:57344
	ds_read_b128 v[74:77], v213 offset:61440
	ds_read_b128 v[78:81], v214 offset:49152
	ds_read_b128 v[82:85], v214 offset:53248
	ds_read_b128 v[86:89], v214 offset:57344
	ds_read_b128 v[90:93], v214 offset:61440
	s_waitcnt lgkmcnt(11)
	v_mfma_f32_32x32x16_bf16 v[142:157], v[34:37], v[190:193], v[142:157]
	s_waitcnt lgkmcnt(10)
	v_mfma_f32_32x32x16_bf16 v[126:141], v[38:41], v[190:193], v[126:141]
	s_waitcnt lgkmcnt(9)
	v_mfma_f32_32x32x16_bf16 v[110:125], v[48:51], v[190:193], v[110:125]
	s_waitcnt lgkmcnt(8)
	v_mfma_f32_32x32x16_bf16 v[94:109], v[52:55], v[190:193], v[94:109]
	ds_read_b128 v[34:37], v215 offset:49152
	ds_read_b128 v[38:41], v215 offset:53248
	ds_read_b128 v[48:51], v215 offset:57344
	ds_read_b128 v[52:55], v215 offset:61440
	s_waitcnt lgkmcnt(11)
	v_mfma_f32_32x32x16_bf16 v[142:157], v[62:65], v[194:197], v[142:157]
	s_waitcnt lgkmcnt(10)
	v_mfma_f32_32x32x16_bf16 v[126:141], v[66:69], v[194:197], v[126:141]
	s_waitcnt lgkmcnt(9)
	v_mfma_f32_32x32x16_bf16 v[110:125], v[70:73], v[194:197], v[110:125]
	s_waitcnt lgkmcnt(8)
	v_mfma_f32_32x32x16_bf16 v[94:109], v[74:77], v[194:197], v[94:109]
	s_waitcnt lgkmcnt(7)
	v_mfma_f32_32x32x16_bf16 v[142:157], v[78:81], v[198:201], v[142:157]
	s_waitcnt lgkmcnt(6)
	v_mfma_f32_32x32x16_bf16 v[126:141], v[82:85], v[198:201], v[126:141]
	s_waitcnt lgkmcnt(5)
	v_mfma_f32_32x32x16_bf16 v[110:125], v[86:89], v[198:201], v[110:125]
	s_waitcnt lgkmcnt(4)
	v_mfma_f32_32x32x16_bf16 v[94:109], v[90:93], v[198:201], v[94:109]
	s_waitcnt lgkmcnt(3)
	v_mfma_f32_32x32x16_bf16 v[142:157], v[34:37], v[202:205], v[142:157]
	s_waitcnt lgkmcnt(2)
	v_mfma_f32_32x32x16_bf16 v[126:141], v[38:41], v[202:205], v[126:141]
	s_waitcnt lgkmcnt(1)
	v_mfma_f32_32x32x16_bf16 v[110:125], v[48:51], v[202:205], v[110:125]
	s_waitcnt lgkmcnt(0)
	v_mfma_f32_32x32x16_bf16 v[94:109], v[52:55], v[202:205], v[94:109]
	s_cmp_eq_u32 s14, s74
	s_cselect_b64 s[12:13], -1, 0
	s_cmp_eq_u32 s24, s74
	s_cselect_b64 s[0:1], -1, 0
	s_or_b64 s[0:1], s[12:13], s[0:1]
	s_andn2_b64 vcc, exec, s[0:1]
	s_cbranch_vccnz .Lpvdone_0
; #define GAS __attribute__((address_space(1)))
; __device__ __forceinline__ unsigned cvt_pk_bf16(float lo, float hi) { unsigned r; asm volatile("v_cvt_pk_bf16_f32 %0, %1, %2" : "=v"(r) : "v"(lo), "v"(hi)); return r; }
; __device__ __forceinline__ void nsa_unit(const Args& a, LAS unsigned char* lds, int b, int kvh, int qb) {
;     ...
;             if (ti == nS - 1 || ti == nTot - 1) {
;                 const float lt = lrun + __shfl_xor(lrun, 32); const float f = ((ti == nS - 1) ? g1 : g2) / lt;
; #pragma unroll
;                 for (int dt = 0; dt < 4; ++dt) {
; #pragma unroll
;                     for (int aa = 0; aa < 4; ++aa) { const u32x2 pv = *(const GAS u32x2*)(mp + (32 * dt + 8 * aa) * 2); u32x2 wv;
;                         wv.x = pg8::cvt_pk_bf16(bflo(pv.x) + o[dt][4 * aa] * f, bfhi(pv.x) + o[dt][4 * aa + 1] * f); wv.y = pg8::cvt_pk_bf16(bflo(pv.y) + o[dt][4 * aa + 2] * f, bfhi(pv.y) + o[dt][4 * aa + 3] * f);
;                         *(GAS u32x2*)(mp + (32 * dt + 8 * aa) * 2) = wv; }
; #pragma unroll
;                     for (int i = 0; i < 16; ++i) o[dt][i] = 0.f; }
;                 mrun = -1e30f; lrun = 0.f;
;                 asm volatile("s_waitcnt vmcnt(0)" ::: "memory");
	ds_bpermute_b32 v229, v252, v209
	v_cndmask_b32_e64 v208, v251, v250, s[12:13]
	v_mov_b32_e32 v60, v47
	v_mov_b32_e32 v61, v47
	v_mov_b32_e32 v48, v47
	s_waitcnt lgkmcnt(0)
	v_pk_add_f32 v[34:35], v[208:209], v[228:229]
	v_mov_b32_e32 v49, v47
	v_div_scale_f32 v36, s[0:1], v34, v34, 1.0
	v_rcp_f32_e32 v37, v36
	v_mov_b32_e32 v50, v47
	v_mov_b32_e32 v51, v47
	v_mov_b32_e32 v52, v47
	v_fma_f32 v38, -v36, v37, 1.0
	v_fmac_f32_e32 v37, v38, v37
	v_div_scale_f32 v38, vcc, 1.0, v34, 1.0
	v_mul_f32_e32 v39, v38, v37
	v_fma_f32 v40, -v36, v39, v38
	v_fmac_f32_e32 v39, v40, v37
	v_fma_f32 v36, -v36, v39, v38
	v_div_fmas_f32 v36, v36, v37, v39
	v_div_fixup_f32 v34, v36, v34, 1.0
	v_div_scale_f32 v36, s[0:1], v35, v35, v34
	v_rcp_f32_e32 v37, v36
	v_mov_b32_e32 v53, v47
	v_mov_b32_e32 v54, v47
	v_mov_b32_e32 v55, v47
	v_fma_f32 v38, -v36, v37, 1.0
	v_fmac_f32_e32 v37, v38, v37
	v_div_scale_f32 v38, vcc, v34, v35, v34
	v_mul_f32_e32 v39, v38, v37
	v_fma_f32 v40, -v36, v39, v38
	v_fmac_f32_e32 v39, v40, v37
	v_fma_f32 v36, -v36, v39, v38
	v_div_fmas_f32 v36, v36, v37, v39
	v_div_fixup_f32 v46, v36, v35, v34
	v_mov_b32_e32 v56, v47
	v_mov_b32_e32 v57, v47
	v_mov_b32_e32 v58, v47
	v_mov_b32_e32 v59, v47
	v_mov_b32_e32 v208, 0xf149f2ca
	v_mov_b32_e32 v209, 0
	global_load_dwordx2 v[62:63], v[206:207], off
	global_load_dwordx2 v[64:65], v[206:207], off offset:16
	global_load_dwordx2 v[66:67], v[206:207], off offset:32
	global_load_dwordx2 v[68:69], v[206:207], off offset:48
	global_load_dwordx2 v[70:71], v[206:207], off offset:64
	global_load_dwordx2 v[72:73], v[206:207], off offset:80
	global_load_dwordx2 v[74:75], v[206:207], off offset:96
	global_load_dwordx2 v[76:77], v[206:207], off offset:112
	global_load_dwordx2 v[78:79], v[206:207], off offset:128
	global_load_dwordx2 v[80:81], v[206:207], off offset:144
	global_load_dwordx2 v[82:83], v[206:207], off offset:160
	global_load_dwordx2 v[84:85], v[206:207], off offset:176
	global_load_dwordx2 v[86:87], v[206:207], off offset:192
	global_load_dwordx2 v[88:89], v[206:207], off offset:208
	global_load_dwordx2 v[90:91], v[206:207], off offset:224
	global_load_dwordx2 v[92:93], v[206:207], off offset:240
	s_waitcnt vmcnt(15)
	v_lshlrev_b32_e32 v36, 16, v62
	v_and_b32_e32 v34, 0xffff0000, v62
	v_fmac_f32_e32 v36, v142, v46
	v_fmac_f32_e32 v34, v143, v46
	v_cvt_pk_bf16_f32 v34, v36, v34
	v_lshlrev_b32_e32 v36, 16, v63
	v_and_b32_e32 v35, 0xffff0000, v63
	v_fmac_f32_e32 v35, v145, v46
	v_fmac_f32_e32 v36, v144, v46
	v_cvt_pk_bf16_f32 v35, v36, v35
	global_store_dwordx2 v[206:207], v[34:35], off
	s_waitcnt vmcnt(15)
	v_lshlrev_b32_e32 v36, 16, v64
	v_and_b32_e32 v34, 0xffff0000, v64
	v_fmac_f32_e32 v36, v146, v46
	v_fmac_f32_e32 v34, v147, v46
	v_cvt_pk_bf16_f32 v34, v36, v34
	v_lshlrev_b32_e32 v36, 16, v65
	v_and_b32_e32 v35, 0xffff0000, v65
	v_fmac_f32_e32 v35, v149, v46
	v_fmac_f32_e32 v36, v148, v46
	v_cvt_pk_bf16_f32 v35, v36, v35
	global_store_dwordx2 v[206:207], v[34:35], off offset:16
	s_waitcnt vmcnt(15)
	v_lshlrev_b32_e32 v36, 16, v66
	v_and_b32_e32 v34, 0xffff0000, v66
	v_fmac_f32_e32 v36, v150, v46
	v_fmac_f32_e32 v34, v151, v46
	v_cvt_pk_bf16_f32 v34, v36, v34
	v_lshlrev_b32_e32 v36, 16, v67
	v_and_b32_e32 v35, 0xffff0000, v67
	v_fmac_f32_e32 v35, v153, v46
	v_fmac_f32_e32 v36, v152, v46
	v_cvt_pk_bf16_f32 v35, v36, v35
	global_store_dwordx2 v[206:207], v[34:35], off offset:32
	s_waitcnt vmcnt(15)
	v_lshlrev_b32_e32 v36, 16, v68
	v_and_b32_e32 v34, 0xffff0000, v68
	v_fmac_f32_e32 v36, v154, v46
	v_fmac_f32_e32 v34, v155, v46
	v_cvt_pk_bf16_f32 v34, v36, v34
	v_lshlrev_b32_e32 v36, 16, v69
	v_and_b32_e32 v35, 0xffff0000, v69
	v_fmac_f32_e32 v35, v157, v46
	v_fmac_f32_e32 v36, v156, v46
	v_cvt_pk_bf16_f32 v35, v36, v35
	global_store_dwordx2 v[206:207], v[34:35], off offset:48
	s_waitcnt vmcnt(15)
	v_lshlrev_b32_e32 v36, 16, v70
	v_and_b32_e32 v34, 0xffff0000, v70
	v_fmac_f32_e32 v36, v126, v46
	v_fmac_f32_e32 v34, v127, v46
	v_cvt_pk_bf16_f32 v34, v36, v34
	v_lshlrev_b32_e32 v36, 16, v71
	v_and_b32_e32 v35, 0xffff0000, v71
	v_fmac_f32_e32 v35, v129, v46
	v_fmac_f32_e32 v36, v128, v46
	v_cvt_pk_bf16_f32 v35, v36, v35
	global_store_dwordx2 v[206:207], v[34:35], off offset:64
	s_waitcnt vmcnt(15)
	v_lshlrev_b32_e32 v36, 16, v72
	v_and_b32_e32 v34, 0xffff0000, v72
	v_fmac_f32_e32 v36, v130, v46
	v_fmac_f32_e32 v34, v131, v46
	v_cvt_pk_bf16_f32 v34, v36, v34
	v_lshlrev_b32_e32 v36, 16, v73
	v_and_b32_e32 v35, 0xffff0000, v73
	v_fmac_f32_e32 v35, v133, v46
	v_fmac_f32_e32 v36, v132, v46
	v_cvt_pk_bf16_f32 v35, v36, v35
	global_store_dwordx2 v[206:207], v[34:35], off offset:80
	s_waitcnt vmcnt(15)
	v_lshlrev_b32_e32 v36, 16, v74
	v_and_b32_e32 v34, 0xffff0000, v74
	v_fmac_f32_e32 v36, v134, v46
	v_fmac_f32_e32 v34, v135, v46
	v_cvt_pk_bf16_f32 v34, v36, v34
	v_lshlrev_b32_e32 v36, 16, v75
	v_and_b32_e32 v35, 0xffff0000, v75
	v_fmac_f32_e32 v35, v137, v46
	v_fmac_f32_e32 v36, v136, v46
	v_cvt_pk_bf16_f32 v35, v36, v35
	global_store_dwordx2 v[206:207], v[34:35], off offset:96
	s_waitcnt vmcnt(15)
	v_lshlrev_b32_e32 v36, 16, v76
	v_and_b32_e32 v34, 0xffff0000, v76
	v_fmac_f32_e32 v36, v138, v46
	v_fmac_f32_e32 v34, v139, v46
	v_cvt_pk_bf16_f32 v34, v36, v34
	v_lshlrev_b32_e32 v36, 16, v77
	v_and_b32_e32 v35, 0xffff0000, v77
	v_fmac_f32_e32 v35, v141, v46
	v_fmac_f32_e32 v36, v140, v46
	v_cvt_pk_bf16_f32 v35, v36, v35
	global_store_dwordx2 v[206:207], v[34:35], off offset:112
	s_waitcnt vmcnt(15)
	v_lshlrev_b32_e32 v36, 16, v78
	v_and_b32_e32 v34, 0xffff0000, v78
	v_fmac_f32_e32 v36, v110, v46
	v_fmac_f32_e32 v34, v111, v46
	v_cvt_pk_bf16_f32 v34, v36, v34
	v_lshlrev_b32_e32 v36, 16, v79
	v_and_b32_e32 v35, 0xffff0000, v79
	v_fmac_f32_e32 v35, v113, v46
	v_fmac_f32_e32 v36, v112, v46
	v_cvt_pk_bf16_f32 v35, v36, v35
	global_store_dwordx2 v[206:207], v[34:35], off offset:128
	s_waitcnt vmcnt(15)
; #define GAS __attribute__((address_space(1)))
; __device__ __forceinline__ unsigned cvt_pk_bf16(float lo, float hi) { unsigned r; asm volatile("v_cvt_pk_bf16_f32 %0, %1, %2" : "=v"(r) : "v"(lo), "v"(hi)); return r; }
; __device__ __forceinline__ void nsa_unit(const Args& a, LAS unsigned char* lds, int b, int kvh, int qb) {
;     ...
;                     for (int aa = 0; aa < 4; ++aa) { const u32x2 pv = *(const GAS u32x2*)(mp + (32 * dt + 8 * aa) * 2); u32x2 wv;
;                         wv.x = pg8::cvt_pk_bf16(bflo(pv.x) + o[dt][4 * aa] * f, bfhi(pv.x) + o[dt][4 * aa + 1] * f); wv.y = pg8::cvt_pk_bf16(bflo(pv.y) + o[dt][4 * aa + 2] * f, bfhi(pv.y) + o[dt][4 * aa + 3] * f);
;                         *(GAS u32x2*)(mp + (32 * dt + 8 * aa) * 2) = wv; }
; #pragma unroll
;                     for (int i = 0; i < 16; ++i) o[dt][i] = 0.f; }
;                 mrun = -1e30f; lrun = 0.f;
	v_lshlrev_b32_e32 v36, 16, v80
	v_and_b32_e32 v34, 0xffff0000, v80
	v_fmac_f32_e32 v36, v114, v46
	v_fmac_f32_e32 v34, v115, v46
	v_cvt_pk_bf16_f32 v34, v36, v34
	v_lshlrev_b32_e32 v36, 16, v81
	v_and_b32_e32 v35, 0xffff0000, v81
	v_fmac_f32_e32 v35, v117, v46
	v_fmac_f32_e32 v36, v116, v46
	v_cvt_pk_bf16_f32 v35, v36, v35
	global_store_dwordx2 v[206:207], v[34:35], off offset:144
	s_waitcnt vmcnt(15)
	v_lshlrev_b32_e32 v36, 16, v82
	v_and_b32_e32 v34, 0xffff0000, v82
	v_fmac_f32_e32 v36, v118, v46
	v_fmac_f32_e32 v34, v119, v46
	v_cvt_pk_bf16_f32 v34, v36, v34
	v_lshlrev_b32_e32 v36, 16, v83
	v_and_b32_e32 v35, 0xffff0000, v83
	v_fmac_f32_e32 v35, v121, v46
	v_fmac_f32_e32 v36, v120, v46
	v_cvt_pk_bf16_f32 v35, v36, v35
	global_store_dwordx2 v[206:207], v[34:35], off offset:160
	s_waitcnt vmcnt(15)
	v_lshlrev_b32_e32 v36, 16, v84
	v_and_b32_e32 v34, 0xffff0000, v84
	v_fmac_f32_e32 v36, v122, v46
	v_fmac_f32_e32 v34, v123, v46
	v_cvt_pk_bf16_f32 v34, v36, v34
	v_lshlrev_b32_e32 v36, 16, v85
	v_and_b32_e32 v35, 0xffff0000, v85
	v_fmac_f32_e32 v35, v125, v46
	v_fmac_f32_e32 v36, v124, v46
	v_cvt_pk_bf16_f32 v35, v36, v35
	global_store_dwordx2 v[206:207], v[34:35], off offset:176
	s_waitcnt vmcnt(15)
	v_lshlrev_b32_e32 v36, 16, v86
	v_and_b32_e32 v34, 0xffff0000, v86
	v_fmac_f32_e32 v36, v94, v46
	v_fmac_f32_e32 v34, v95, v46
	v_cvt_pk_bf16_f32 v34, v36, v34
	v_lshlrev_b32_e32 v36, 16, v87
	v_and_b32_e32 v35, 0xffff0000, v87
	v_fmac_f32_e32 v35, v97, v46
	v_fmac_f32_e32 v36, v96, v46
	v_cvt_pk_bf16_f32 v35, v36, v35
	global_store_dwordx2 v[206:207], v[34:35], off offset:192
	s_waitcnt vmcnt(15)
	v_lshlrev_b32_e32 v36, 16, v88
	v_and_b32_e32 v34, 0xffff0000, v88
	v_fmac_f32_e32 v36, v98, v46
	v_fmac_f32_e32 v34, v99, v46
	v_cvt_pk_bf16_f32 v34, v36, v34
	v_lshlrev_b32_e32 v36, 16, v89
	v_and_b32_e32 v35, 0xffff0000, v89
	v_fmac_f32_e32 v35, v101, v46
	v_fmac_f32_e32 v36, v100, v46
	v_cvt_pk_bf16_f32 v35, v36, v35
	global_store_dwordx2 v[206:207], v[34:35], off offset:208
	s_waitcnt vmcnt(15)
	v_lshlrev_b32_e32 v36, 16, v90
	v_and_b32_e32 v34, 0xffff0000, v90
	v_fmac_f32_e32 v36, v102, v46
	v_fmac_f32_e32 v34, v103, v46
	v_cvt_pk_bf16_f32 v34, v36, v34
	v_lshlrev_b32_e32 v36, 16, v91
	v_and_b32_e32 v35, 0xffff0000, v91
	v_fmac_f32_e32 v35, v105, v46
	v_fmac_f32_e32 v36, v104, v46
	v_cvt_pk_bf16_f32 v35, v36, v35
	global_store_dwordx2 v[206:207], v[34:35], off offset:224
	s_waitcnt vmcnt(15)
	v_lshlrev_b32_e32 v36, 16, v92
	v_and_b32_e32 v34, 0xffff0000, v92
	v_fmac_f32_e32 v36, v106, v46
	v_fmac_f32_e32 v34, v107, v46
	v_cvt_pk_bf16_f32 v34, v36, v34
	v_lshlrev_b32_e32 v36, 16, v93
	v_and_b32_e32 v35, 0xffff0000, v93
	v_fmac_f32_e32 v35, v109, v46
	v_fmac_f32_e32 v36, v108, v46
	v_cvt_pk_bf16_f32 v35, v36, v35
	global_store_dwordx2 v[206:207], v[34:35], off offset:240
	s_waitcnt vmcnt(0)
	v_mov_b32_e32 v46, v47
	v_mov_b64_e32 v[156:157], v[60:61]
	v_mov_b64_e32 v[140:141], v[60:61]
	v_mov_b64_e32 v[124:125], v[60:61]
	v_mov_b64_e32 v[108:109], v[60:61]
	v_mov_b64_e32 v[154:155], v[58:59]
	v_mov_b64_e32 v[152:153], v[56:57]
	v_mov_b64_e32 v[150:151], v[54:55]
	v_mov_b64_e32 v[148:149], v[52:53]
	v_mov_b64_e32 v[146:147], v[50:51]
	v_mov_b64_e32 v[144:145], v[48:49]
	v_mov_b64_e32 v[142:143], v[46:47]
	v_mov_b64_e32 v[138:139], v[58:59]
	v_mov_b64_e32 v[136:137], v[56:57]
	v_mov_b64_e32 v[134:135], v[54:55]
	v_mov_b64_e32 v[132:133], v[52:53]
	v_mov_b64_e32 v[130:131], v[50:51]
	v_mov_b64_e32 v[128:129], v[48:49]
	v_mov_b64_e32 v[126:127], v[46:47]
	v_mov_b64_e32 v[122:123], v[58:59]
	v_mov_b64_e32 v[120:121], v[56:57]
	v_mov_b64_e32 v[118:119], v[54:55]
	v_mov_b64_e32 v[116:117], v[52:53]
	v_mov_b64_e32 v[114:115], v[50:51]
	v_mov_b64_e32 v[112:113], v[48:49]
	v_mov_b64_e32 v[110:111], v[46:47]
	v_mov_b64_e32 v[106:107], v[58:59]
	v_mov_b64_e32 v[104:105], v[56:57]
	v_mov_b64_e32 v[102:103], v[54:55]
	v_mov_b64_e32 v[100:101], v[52:53]
	v_mov_b64_e32 v[98:99], v[50:51]
	v_mov_b64_e32 v[96:97], v[48:49]
	v_mov_b64_e32 v[94:95], v[46:47]
; #define LAS __attribute__((address_space(3)))
; __device__ __forceinline__ void nsa_dma_tile(const bf16* kt, unsigned kstr, const bf16* vt, unsigned vstr, unsigned ldsK, unsigned ldsV, int w, int lane) {
; #pragma unroll
;     for (int i = 0; i < 2; ++i) { const int q = 2 * w + i, row = 4 * q + (lane >> 4), c = (lane & 15) ^ (row & 15);
;         glds16((const unsigned char*)kt + ((size_t)row * kstr + c * 16), (unsigned)__builtin_amdgcn_readfirstlane((int)(ldsK + q * 1024))); }
; #pragma unroll
;     for (int i = 0; i < 2; ++i) { const int q = 2 * w + i, row = 8 * q + (lane >> 3), c = (lane & 7) ^ ((row >> 1) & 7);
;         glds16((const unsigned char*)vt + ((size_t)row * vstr + c * 16), (unsigned)__builtin_amdgcn_readfirstlane((int)(ldsV + q * 1024))); }
; }
; __device__ __forceinline__ void nsa_qk_sw(const LAS unsigned char* kbuf, const bf16x8 (&qf)[8], int r, int h, f32x16& p0, f32x16& p1) {
;     const int x = r & 15; const LAS unsigned char* kA = kbuf + r * 256 + ((h ^ (x & 1)) * 16); const int xk = (x & 14) * 16;
; #pragma unroll
;     for (int i = 0; i < 16; ++i) { p0[i] = 0.f; p1[i] = 0.f; }
;     bf16x8 a0, a1, b0, b1;
;     a0 = *(const LAS bf16x8*)(kA + (0 ^ xk)); a1 = *(const LAS bf16x8*)(kA + (0 ^ xk) + 8192); __builtin_amdgcn_sched_barrier(0);
; #pragma unroll
;     for (int ks = 0; ks < 8; ks += 2) {
;         b0 = *(const LAS bf16x8*)(kA + (((ks + 1) * 32) ^ xk)); b1 = *(const LAS bf16x8*)(kA + (((ks + 1) * 32) ^ xk) + 8192); __builtin_amdgcn_sched_barrier(0);
;         p0 = __builtin_amdgcn_mfma_f32_32x32x16_bf16(a0, qf[ks], p0, 0, 0, 0); p1 = __builtin_amdgcn_mfma_f32_32x32x16_bf16(a1, qf[ks], p1, 0, 0, 0); __builtin_amdgcn_sched_barrier(0);
;         if (ks + 2 < 8) { a0 = *(const LAS bf16x8*)(kA + (((ks + 2) * 32) ^ xk)); a1 = *(const LAS bf16x8*)(kA + (((ks + 2) * 32) ^ xk) + 8192); } __builtin_amdgcn_sched_barrier(0);
; __device__ __forceinline__ void nsa_unit(const Args& a, LAS unsigned char* lds, int b, int kvh, int qb) {
;     ...
;         asm volatile("s_waitcnt lgkmcnt(0)\n\ts_barrier" ::: "memory");
;         if (it + 2 < nTot) { const bf16 *kt, *vt; tile_src(it + 2, kt, vt); const int t2 = it + 2;
;             int lo_ = lane; asm volatile("" : "+v"(lo_)); nsa_dma_tile(kt, PW * 2, vt, VTP * 2, ldsb + (t2 % 3) * NTB, ldsb + VOFF + (t2 & 3) * NTB, w, lo_); }
.Lpvdone_0:
.LBB0_912:
	s_waitcnt lgkmcnt(0)
	s_barrier
	s_add_i32 s2, s74, 2
	s_cmp_gt_i32 s2, s15
	s_cbranch_scc1 .LBB0_914
	s_mul_hi_u32 s3, s62, 0xaaaaaaab
	s_lshr_b32 s3, s3, 1
	s_mul_i32 s3, s3, 0xc000
	s_sub_i32 s33, s18, s3
	s_cmp_gt_i32 s2, s72
	s_cselect_b64 s[2:3], -1, 0
	s_and_b64 s[4:5], s[2:3], exec
	s_cselect_b32 s4, s16, 0
	s_cselect_b32 s13, s95, s91
	s_cselect_b32 s12, s94, s90
	s_add_i32 s4, s4, s74
	s_lshl_b32 s4, s4, 6
	s_addk_i32 s4, 0x80
	s_ashr_i32 s5, s4, 31
	s_mul_i32 vcc_hi, s4, 0x2e00
	s_mul_hi_i32 vcc_lo, s4, 0x2e00
	s_add_u32 s12, s12, vcc_hi
	s_addc_u32 s13, s13, vcc_lo
	s_and_b64 s[2:3], s[2:3], exec
	v_mov_b32_e32 v38, v45
	s_cselect_b32 vcc_lo, s70, s97
	s_cselect_b32 vcc_hi, s69, s96
	s_lshl_b64 s[2:3], s[4:5], 1
	s_add_u32 s2, vcc_hi, s2
	v_ashrrev_i32_e32 v39, 4, v38
	v_add_u32_e32 v36, s73, v39
	s_addc_u32 s3, vcc_lo, s3
	s_add_i32 s4, s75, 0xc000
	v_xor_b32_e32 v34, v36, v38
	s_and_b32 s4, s4, 0xc000
	v_lshlrev_b32_e32 v34, 4, v34
	s_add_i32 s4, s4, 0
	v_and_b32_e32 v46, 0xf0, v34
	v_mov_b64_e32 v[34:35], s[12:13]
	s_add_i32 vcc_lo, s4, 0xc000
	v_mad_i64_i32 v[36:37], s[4:5], v36, s77, v[34:35]
	v_lshl_add_u64 v[36:37], v[36:37], 0, v[46:47]
	s_add_i32 s12, s75, s33
	s_add_i32 s4, s12, 0xc000
	s_mov_b32 s5, m0
	s_mov_b32 m0, s4
	s_nop 0
	global_load_lds_dwordx4 v[36:37], off
	s_mov_b32 m0, s5
	v_add_u32_e32 v36, s19, v39
	v_xor_b32_e32 v37, v36, v38
	v_lshlrev_b32_e32 v37, 4, v37
	v_and_b32_e32 v46, 0xf0, v37
	v_mad_i64_i32 v[34:35], s[4:5], v36, s77, v[34:35]
	v_lshl_add_u64 v[34:35], v[34:35], 0, v[46:47]
	v_ashrrev_i32_e32 v39, 3, v38
	s_add_i32 s4, s12, 0xc400
	s_mov_b32 s5, m0
	s_mov_b32 m0, s4
	s_nop 0
	global_load_lds_dwordx4 v[34:35], off
	s_mov_b32 m0, s5
	v_lshrrev_b32_e32 v34, 1, v39
	v_xor_b32_e32 v34, v34, v38
	v_lshlrev_b32_e32 v34, 4, v34
	v_add_u32_e32 v36, s21, v39
	v_and_b32_e32 v46, 0x70, v34
	v_mov_b64_e32 v[34:35], s[2:3]
	v_mad_i64_i32 v[36:37], s[2:3], v36, s78, v[34:35]
	v_lshl_add_u64 v[36:37], v[36:37], 0, v[46:47]
	s_add_i32 s2, vcc_lo, s17
	s_mov_b32 s3, m0
	s_mov_b32 m0, s2
	s_nop 0
	global_load_lds_dwordx4 v[36:37], off
	s_mov_b32 m0, s3
	v_add_u32_e32 v36, s22, v39
	v_lshrrev_b32_e32 v37, 1, v36
	v_xor_b32_e32 v37, v37, v38
	v_lshlrev_b32_e32 v37, 4, v37
	v_and_b32_e32 v46, 0x70, v37
	v_mad_i64_i32 v[34:35], s[2:3], v36, s78, v[34:35]
	v_lshl_add_u64 v[34:35], v[34:35], 0, v[46:47]
	s_add_i32 s2, vcc_lo, s20
	s_mov_b32 s3, m0
	s_mov_b32 m0, s2
	s_nop 0
	global_load_lds_dwordx4 v[34:35], off
	s_mov_b32 m0, s3
.LBB0_914:
	v_mov_b32_e32 v211, v233
	v_mov_b32_e32 v210, v232
.LBB0_917:
	s_cmp_gt_i32 s74, s15
	s_cbranch_scc1 .LBB0_896
	s_mul_hi_u32 s0, s74, 0xaaaaaaab
	s_lshr_b32 s0, s0, 1
	v_lshlrev_b32_e32 v57, 4, v210
	s_mul_i32 s0, s0, 0xffff4000
	v_lshlrev_b32_e32 v46, 8, v210
	v_bitop3_b32 v34, v210, v211, 1 bitop3:0x6c
	v_and_b32_e32 v58, 0xe0, v57
	s_add_i32 s1, s75, 0
	v_lshlrev_b32_e32 v56, 4, v34
	s_add_i32 s1, s1, s0
	v_or_b32_e32 v220, v46, v58
	v_add3_u32 v220, v220, v56, s1
	ds_read_b128 v[34:37], v220 offset:16384
	ds_read_b128 v[38:41], v220 offset:24576
	v_bitop3_b32 v221, v58, v46, 32 bitop3:0xde
	v_add3_u32 v221, v221, v56, s1
	ds_read_b128 v[48:51], v221 offset:16384
	ds_read_b128 v[52:55], v221 offset:24576
	v_bitop3_b32 v220, v58, v46, 64 bitop3:0xde
	v_add3_u32 v220, v220, v56, s1
	ds_read_b128 v[212:215], v220 offset:16384
	ds_read_b128 v[216:219], v220 offset:24576
	s_waitcnt lgkmcnt(5)
	v_mfma_f32_32x32x16_bf16 v[78:93], v[34:37], v[182:185], 0
	s_waitcnt lgkmcnt(4)
	v_mfma_f32_32x32x16_bf16 v[62:77], v[38:41], v[182:185], 0
	v_bitop3_b32 v221, v58, v46, s68 bitop3:0xde
	v_add3_u32 v221, v221, v56, s1
	ds_read_b128 v[34:37], v221 offset:16384
	ds_read_b128 v[38:41], v221 offset:24576
	s_waitcnt lgkmcnt(5)
	v_mfma_f32_32x32x16_bf16 v[78:93], v[48:51], v[186:189], v[78:93]
	s_waitcnt lgkmcnt(4)
	v_mfma_f32_32x32x16_bf16 v[62:77], v[52:55], v[186:189], v[62:77]
	s_movk_i32 s0, 0x80
	v_bitop3_b32 v220, v58, v46, s0 bitop3:0xde
	v_add3_u32 v220, v220, v56, s1
	ds_read_b128 v[48:51], v220 offset:16384
	ds_read_b128 v[52:55], v220 offset:24576
	s_waitcnt lgkmcnt(5)
	v_mfma_f32_32x32x16_bf16 v[78:93], v[212:215], v[158:161], v[78:93]
	s_waitcnt lgkmcnt(4)
	v_mfma_f32_32x32x16_bf16 v[62:77], v[216:219], v[158:161], v[62:77]
	s_movk_i32 s0, 0xa0
	v_bitop3_b32 v221, v58, v46, s0 bitop3:0xde
	v_add3_u32 v221, v221, v56, s1
	ds_read_b128 v[212:215], v221 offset:16384
	ds_read_b128 v[216:219], v221 offset:24576
	s_waitcnt lgkmcnt(5)
	v_mfma_f32_32x32x16_bf16 v[78:93], v[34:37], v[162:165], v[78:93]
	s_waitcnt lgkmcnt(4)
	v_mfma_f32_32x32x16_bf16 v[62:77], v[38:41], v[162:165], v[62:77]
	s_movk_i32 s0, 0xc0
	v_bitop3_b32 v220, v58, v46, s0 bitop3:0xde
	v_add3_u32 v220, v220, v56, s1
	ds_read_b128 v[34:37], v220 offset:16384
	ds_read_b128 v[38:41], v220 offset:24576
	s_waitcnt lgkmcnt(5)
	v_mfma_f32_32x32x16_bf16 v[78:93], v[48:51], v[166:169], v[78:93]
	s_waitcnt lgkmcnt(4)
	v_mfma_f32_32x32x16_bf16 v[62:77], v[52:55], v[166:169], v[62:77]
	s_movk_i32 s0, 0xe0
	v_bitop3_b32 v221, v57, v46, s0 bitop3:0xce
	v_add3_u32 v221, v221, v56, s1
	ds_read_b128 v[48:51], v221 offset:16384
	ds_read_b128 v[52:55], v221 offset:24576
	s_waitcnt lgkmcnt(5)
	v_mfma_f32_32x32x16_bf16 v[78:93], v[212:215], v[170:173], v[78:93]
	s_waitcnt lgkmcnt(4)
	v_mfma_f32_32x32x16_bf16 v[62:77], v[216:219], v[170:173], v[62:77]
	s_waitcnt lgkmcnt(3)
	v_mfma_f32_32x32x16_bf16 v[78:93], v[34:37], v[174:177], v[78:93]
	s_waitcnt lgkmcnt(2)
	v_mfma_f32_32x32x16_bf16 v[62:77], v[38:41], v[174:177], v[62:77]
	s_waitcnt lgkmcnt(1)
	v_mfma_f32_32x32x16_bf16 v[78:93], v[48:51], v[178:181], v[78:93]
	s_waitcnt lgkmcnt(0)
	v_mfma_f32_32x32x16_bf16 v[62:77], v[52:55], v[178:181], v[62:77]
	s_branch .LBB0_896

; #define LAS __attribute__((address_space(3)))
; __device__ __forceinline__ void nsa_pv_rd4(const LAS unsigned char* vA, int sv, int step, bf16x8 (&af)[4]) {
; #pragma unroll
;     for (int dt = 0; dt < 4; ++dt) af[dt] = *(const LAS bf16x8*)(vA + dt * 4096 + (((2 * step) * 16) ^ sv));
; }
; __device__ __forceinline__ void nsa_pv_mm4(const bf16x8 (&af)[4], const bf16x8& pfk, f32x16 (&o)[4]) {
; #pragma unroll
;     for (int dt = 0; dt < 4; ++dt) o[dt] = __builtin_amdgcn_mfma_f32_32x32x16_bf16(af[dt], pfk, o[dt], 0, 0, 0);
; }
; __device__ __forceinline__ void nsa_pv_sw(const LAS unsigned char* vbuf, const bf16x8 (&pf)[2][2], f32x16 (&o)[4], int r, int h) {
;     const int sv = (((r >> 1) & 7) ^ h) * 16; const LAS unsigned char* vA = vbuf + r * 128;
; #pragma unroll
;     for (int step = 0; step < 4; ++step) { bf16x8 fa[4];
;         nsa_pv_rd4(vA, sv, step, fa); __builtin_amdgcn_sched_barrier(0);
;         nsa_pv_mm4(fa, pf[step >> 1][step & 1], o); __builtin_amdgcn_sched_barrier(0); }
; __device__ __forceinline__ void nsa_unit(const Args& a, LAS unsigned char* lds, int b, int kvh, int qb) {
;     ...
;             const float nmc = lane_on ? -mrun * SM_C : NINF;
;             float ls = 0.f;
; #pragma unroll
;             for (int i = 0; i < 16; ++i) { p0[i] = __builtin_amdgcn_exp2f(fmaf(p0[i], SM_C, nmc)); p1[i] = __builtin_amdgcn_exp2f(fmaf(p1[i], SM_C, nmc)); ls += p0[i] + p1[i]; }
;             lrun = lrun * alpha + ls;
;             pf[0][0] = nsa_pack8(p0, 0); pf[0][1] = nsa_pack8(p0, 1); pf[1][0] = nsa_pack8(p1, 0); pf[1][1] = nsa_pack8(p1, 1);
;         }
;         asm volatile("s_waitcnt lgkmcnt(0)\n\ts_barrier" ::: "memory");
;         if (it + 2 < nTot) { const bf16 *kt, *vt; tile_src(it + 2, kt, vt); const int t2 = it + 2;
;             int lo_ = lane; asm volatile("" : "+v"(lo_)); nsa_dma_tile(kt, PW * 2, vt, VTP * 2, ldsb + (t2 % 3) * NTB, ldsb + VOFF + (t2 & 3) * NTB, w, lo_); }
;         int ro = r, ho = h; asm volatile("" : "+v"(ro), "+v"(ho));
;         if (it > 0) { const int ti = it - 1;
;             nsa_pv_sw(lds + VOFF + (ti & 3) * NTB, pf, o, ro, ho);
;             if (ti == nS - 1 || ti == nTot - 1) {
.LBB0_1857:
	v_mul_f32_e32 v34, 0xbe0293ee, v208
	v_cndmask_b32_e64 v190, v244, v34, s[2:3]
	v_fmamk_f32 v34, v78, 0x3e0293ee, v190
	v_exp_f32_e32 v78, v34
	v_fmamk_f32 v34, v62, 0x3e0293ee, v190
	v_exp_f32_e32 v62, v34
	v_fmamk_f32 v34, v79, 0x3e0293ee, v190
	v_fmamk_f32 v36, v80, 0x3e0293ee, v190
	v_exp_f32_e32 v79, v34
	v_fmamk_f32 v34, v63, 0x3e0293ee, v190
	v_exp_f32_e32 v80, v36
	v_fmamk_f32 v36, v64, 0x3e0293ee, v190
	v_exp_f32_e32 v63, v34
	v_exp_f32_e32 v64, v36
	v_fmamk_f32 v36, v81, 0x3e0293ee, v190
	v_exp_f32_e32 v81, v36
	v_fmamk_f32 v36, v65, 0x3e0293ee, v190
	v_exp_f32_e32 v65, v36
	v_add_f32_e32 v34, v78, v62
	v_add_f32_e32 v34, 0, v34
	v_add_f32_e32 v35, v79, v63
	v_add_f32_e32 v34, v35, v34
	v_add_f32_e32 v35, v80, v64
	v_add_f32_e32 v34, v35, v34
	v_add_f32_e32 v35, v81, v65
	v_add_f32_e32 v50, v35, v34
	v_fmamk_f32 v34, v82, 0x3e0293ee, v190
	v_exp_f32_e32 v35, v34
	v_fmamk_f32 v34, v66, 0x3e0293ee, v190
	v_exp_f32_e32 v37, v34
	v_fmamk_f32 v34, v83, 0x3e0293ee, v190
	v_fmamk_f32 v36, v67, 0x3e0293ee, v190
	v_fmamk_f32 v38, v84, 0x3e0293ee, v190
	v_exp_f32_e32 v34, v34
	v_exp_f32_e32 v36, v36
	v_exp_f32_e32 v39, v38
	v_fmamk_f32 v38, v68, 0x3e0293ee, v190
	v_exp_f32_e32 v41, v38
	v_fmamk_f32 v38, v85, 0x3e0293ee, v190
	v_fmamk_f32 v40, v69, 0x3e0293ee, v190
	v_exp_f32_e32 v38, v38
	v_exp_f32_e32 v40, v40
	v_pk_add_f32 v[48:49], v[34:35], v[36:37]
	v_fmamk_f32 v52, v88, 0x3e0293ee, v190
	v_add_f32_e32 v49, v49, v50
	v_add_f32_e32 v50, v48, v49
	v_pk_add_f32 v[48:49], v[38:39], v[40:41]
	v_exp_f32_e32 v53, v52
	v_add_f32_e32 v49, v49, v50
	v_add_f32_e32 v58, v48, v49
	v_fmamk_f32 v48, v86, 0x3e0293ee, v190
	v_exp_f32_e32 v49, v48
	v_fmamk_f32 v48, v70, 0x3e0293ee, v190
	v_exp_f32_e32 v51, v48
	v_fmamk_f32 v48, v87, 0x3e0293ee, v190
	v_fmamk_f32 v50, v71, 0x3e0293ee, v190
	v_exp_f32_e32 v48, v48
	v_exp_f32_e32 v50, v50
	v_fmamk_f32 v52, v72, 0x3e0293ee, v190
	v_exp_f32_e32 v55, v52
	v_fmamk_f32 v52, v89, 0x3e0293ee, v190
	v_fmamk_f32 v54, v73, 0x3e0293ee, v190
	v_exp_f32_e32 v52, v52
	v_exp_f32_e32 v54, v54
	v_pk_add_f32 v[56:57], v[48:49], v[50:51]
	v_fmamk_f32 v60, v92, 0x3e0293ee, v190
	v_add_f32_e32 v57, v57, v58
	v_add_f32_e32 v58, v56, v57
	v_pk_add_f32 v[56:57], v[52:53], v[54:55]
	v_exp_f32_e32 v61, v60
	v_add_f32_e32 v57, v57, v58
	v_add_f32_e32 v68, v56, v57
	v_fmamk_f32 v56, v90, 0x3e0293ee, v190
	v_exp_f32_e32 v57, v56
	v_fmamk_f32 v56, v74, 0x3e0293ee, v190
	v_exp_f32_e32 v59, v56
	v_fmamk_f32 v56, v91, 0x3e0293ee, v190
	v_fmamk_f32 v58, v75, 0x3e0293ee, v190
	v_exp_f32_e32 v56, v56
	v_exp_f32_e32 v58, v58
	v_fmamk_f32 v60, v76, 0x3e0293ee, v190
	v_exp_f32_e32 v211, v60
	v_fmamk_f32 v60, v93, 0x3e0293ee, v190
	v_fmac_f32_e32 v190, 0x3e0293ee, v77
	v_exp_f32_e32 v60, v60
	v_exp_f32_e32 v210, v190
	v_pk_add_f32 v[66:67], v[56:57], v[58:59]
	v_add_f32_e32 v67, v67, v68
	v_add_f32_e32 v66, v66, v67
	v_pk_add_f32 v[190:191], v[60:61], v[210:211]
	v_add_f32_e32 v191, v191, v66
	v_add_f32_e32 v212, v190, v191
	v_fmac_f32_e32 v212, v209, v46
	v_mov_b32_e32 v209, v212
	v_cvt_pk_bf16_f32 v190, v78, v79
	v_cvt_pk_bf16_f32 v191, v80, v81
	v_cvt_pk_bf16_f32 v192, v35, v34
	v_cvt_pk_bf16_f32 v193, v39, v38
	v_cvt_pk_bf16_f32 v194, v49, v48
	v_cvt_pk_bf16_f32 v195, v53, v52
	v_cvt_pk_bf16_f32 v196, v57, v56
	v_cvt_pk_bf16_f32 v197, v61, v60
	v_cvt_pk_bf16_f32 v198, v62, v63
	v_cvt_pk_bf16_f32 v199, v64, v65
	v_cvt_pk_bf16_f32 v200, v37, v36
	v_cvt_pk_bf16_f32 v201, v41, v40
	v_cvt_pk_bf16_f32 v202, v51, v50
	v_cvt_pk_bf16_f32 v203, v55, v54
	v_cvt_pk_bf16_f32 v204, v59, v58
	v_cvt_pk_bf16_f32 v205, v211, v210
	v_mov_b32_e32 v210, v222
	v_mov_b32_e32 v211, v45
	s_and_b32 s0, s71, 0xc000
	v_lshrrev_b32_e32 v34, 1, v210
	s_add_i32 s0, s0, 0
	v_bitop3_b32 v34, v34, v211, 7 bitop3:0x6c
	v_lshlrev_b32_e32 v46, 4, v34
	v_lshl_add_u32 v56, v210, 7, s0
	v_add_u32_e32 v212, v56, v46
	v_xad_u32 v213, v46, 32, v56
	v_xad_u32 v214, v46, 64, v56
	v_xad_u32 v215, v46, s60, v56
	ds_read_b128 v[34:37], v212 offset:49152
	ds_read_b128 v[38:41], v212 offset:53248
	ds_read_b128 v[48:51], v212 offset:57344
	ds_read_b128 v[52:55], v212 offset:61440
	ds_read_b128 v[62:65], v213 offset:49152
	ds_read_b128 v[66:69], v213 offset:53248
	ds_read_b128 v[70:73], v213 offset:57344
	ds_read_b128 v[74:77], v213 offset:61440
	ds_read_b128 v[78:81], v214 offset:49152
	ds_read_b128 v[82:85], v214 offset:53248
	ds_read_b128 v[86:89], v214 offset:57344
	ds_read_b128 v[90:93], v214 offset:61440
	s_waitcnt lgkmcnt(11)
	v_mfma_f32_32x32x16_bf16 v[142:157], v[34:37], v[190:193], v[142:157]
	s_waitcnt lgkmcnt(10)
	v_mfma_f32_32x32x16_bf16 v[126:141], v[38:41], v[190:193], v[126:141]
	s_waitcnt lgkmcnt(9)
	v_mfma_f32_32x32x16_bf16 v[110:125], v[48:51], v[190:193], v[110:125]
	s_waitcnt lgkmcnt(8)
	v_mfma_f32_32x32x16_bf16 v[94:109], v[52:55], v[190:193], v[94:109]
	ds_read_b128 v[34:37], v215 offset:49152
	ds_read_b128 v[38:41], v215 offset:53248
	ds_read_b128 v[48:51], v215 offset:57344
	ds_read_b128 v[52:55], v215 offset:61440
	s_waitcnt lgkmcnt(11)
	v_mfma_f32_32x32x16_bf16 v[142:157], v[62:65], v[194:197], v[142:157]
	s_waitcnt lgkmcnt(10)
	v_mfma_f32_32x32x16_bf16 v[126:141], v[66:69], v[194:197], v[126:141]
	s_waitcnt lgkmcnt(9)
	v_mfma_f32_32x32x16_bf16 v[110:125], v[70:73], v[194:197], v[110:125]
	s_waitcnt lgkmcnt(8)
	v_mfma_f32_32x32x16_bf16 v[94:109], v[74:77], v[194:197], v[94:109]
	s_waitcnt lgkmcnt(7)
	v_mfma_f32_32x32x16_bf16 v[142:157], v[78:81], v[198:201], v[142:157]
	s_waitcnt lgkmcnt(6)
	v_mfma_f32_32x32x16_bf16 v[126:141], v[82:85], v[198:201], v[126:141]
	s_waitcnt lgkmcnt(5)
	v_mfma_f32_32x32x16_bf16 v[110:125], v[86:89], v[198:201], v[110:125]
	s_waitcnt lgkmcnt(4)
	v_mfma_f32_32x32x16_bf16 v[94:109], v[90:93], v[198:201], v[94:109]
	s_waitcnt lgkmcnt(3)
	v_mfma_f32_32x32x16_bf16 v[142:157], v[34:37], v[202:205], v[142:157]
	s_waitcnt lgkmcnt(2)
	v_mfma_f32_32x32x16_bf16 v[126:141], v[38:41], v[202:205], v[126:141]
	s_waitcnt lgkmcnt(1)
	v_mfma_f32_32x32x16_bf16 v[110:125], v[48:51], v[202:205], v[110:125]
	s_waitcnt lgkmcnt(0)
	v_mfma_f32_32x32x16_bf16 v[94:109], v[52:55], v[202:205], v[94:109]
	s_cmp_eq_u32 s16, s70
	s_cselect_b64 s[12:13], -1, 0
	s_cmp_eq_u32 s57, s70
	s_cselect_b64 s[0:1], -1, 0
	s_or_b64 s[0:1], s[12:13], s[0:1]
	s_andn2_b64 vcc, exec, s[0:1]
	s_cbranch_vccnz .Lpvdone_1
; #define GAS __attribute__((address_space(1)))
; __device__ __forceinline__ unsigned cvt_pk_bf16(float lo, float hi) { unsigned r; asm volatile("v_cvt_pk_bf16_f32 %0, %1, %2" : "=v"(r) : "v"(lo), "v"(hi)); return r; }
; __device__ __forceinline__ void nsa_unit(const Args& a, LAS unsigned char* lds, int b, int kvh, int qb) {
;     ...
;             if (ti == nS - 1 || ti == nTot - 1) {
;                 const float lt = lrun + __shfl_xor(lrun, 32); const float f = ((ti == nS - 1) ? g1 : g2) / lt;
; #pragma unroll
;                 for (int dt = 0; dt < 4; ++dt) {
; #pragma unroll
;                     for (int aa = 0; aa < 4; ++aa) { const u32x2 pv = *(const GAS u32x2*)(mp + (32 * dt + 8 * aa) * 2); u32x2 wv;
;                         wv.x = pg8::cvt_pk_bf16(bflo(pv.x) + o[dt][4 * aa] * f, bfhi(pv.x) + o[dt][4 * aa + 1] * f); wv.y = pg8::cvt_pk_bf16(bflo(pv.y) + o[dt][4 * aa + 2] * f, bfhi(pv.y) + o[dt][4 * aa + 3] * f);
;                         *(GAS u32x2*)(mp + (32 * dt + 8 * aa) * 2) = wv; }
; #pragma unroll
;                     for (int i = 0; i < 16; ++i) o[dt][i] = 0.f; }
;                 mrun = -1e30f; lrun = 0.f;
;                 asm volatile("s_waitcnt vmcnt(0)" ::: "memory");
	ds_bpermute_b32 v233, v252, v209
	v_cndmask_b32_e64 v208, v251, v250, s[12:13]
	v_mov_b32_e32 v60, v47
	v_mov_b32_e32 v61, v47
	v_mov_b32_e32 v48, v47
	s_waitcnt lgkmcnt(0)
	v_pk_add_f32 v[34:35], v[208:209], v[232:233]
	v_mov_b32_e32 v49, v47
	v_div_scale_f32 v36, s[0:1], v34, v34, 1.0
	v_rcp_f32_e32 v37, v36
	v_mov_b32_e32 v50, v47
	v_mov_b32_e32 v51, v47
	v_mov_b32_e32 v52, v47
	v_fma_f32 v38, -v36, v37, 1.0
	v_fmac_f32_e32 v37, v38, v37
	v_div_scale_f32 v38, vcc, 1.0, v34, 1.0
	v_mul_f32_e32 v39, v38, v37
	v_fma_f32 v40, -v36, v39, v38
	v_fmac_f32_e32 v39, v40, v37
	v_fma_f32 v36, -v36, v39, v38
	v_div_fmas_f32 v36, v36, v37, v39
	v_div_fixup_f32 v34, v36, v34, 1.0
	v_div_scale_f32 v36, s[0:1], v35, v35, v34
	v_rcp_f32_e32 v37, v36
	v_mov_b32_e32 v53, v47
	v_mov_b32_e32 v54, v47
	v_mov_b32_e32 v55, v47
	v_fma_f32 v38, -v36, v37, 1.0
	v_fmac_f32_e32 v37, v38, v37
	v_div_scale_f32 v38, vcc, v34, v35, v34
	v_mul_f32_e32 v39, v38, v37
	v_fma_f32 v40, -v36, v39, v38
	v_fmac_f32_e32 v39, v40, v37
	v_fma_f32 v36, -v36, v39, v38
	v_div_fmas_f32 v36, v36, v37, v39
	v_div_fixup_f32 v46, v36, v35, v34
	v_mov_b32_e32 v56, v47
	v_mov_b32_e32 v57, v47
	v_mov_b32_e32 v58, v47
	v_mov_b32_e32 v59, v47
	v_mov_b32_e32 v208, 0xf149f2ca
	v_mov_b32_e32 v209, 0
	global_load_dwordx2 v[62:63], v[206:207], off
	global_load_dwordx2 v[64:65], v[206:207], off offset:16
	global_load_dwordx2 v[66:67], v[206:207], off offset:32
	global_load_dwordx2 v[68:69], v[206:207], off offset:48
	global_load_dwordx2 v[70:71], v[206:207], off offset:64
	global_load_dwordx2 v[72:73], v[206:207], off offset:80
	global_load_dwordx2 v[74:75], v[206:207], off offset:96
	global_load_dwordx2 v[76:77], v[206:207], off offset:112
	global_load_dwordx2 v[78:79], v[206:207], off offset:128
	global_load_dwordx2 v[80:81], v[206:207], off offset:144
	global_load_dwordx2 v[82:83], v[206:207], off offset:160
	global_load_dwordx2 v[84:85], v[206:207], off offset:176
	global_load_dwordx2 v[86:87], v[206:207], off offset:192
	global_load_dwordx2 v[88:89], v[206:207], off offset:208
	global_load_dwordx2 v[90:91], v[206:207], off offset:224
	global_load_dwordx2 v[92:93], v[206:207], off offset:240
	s_waitcnt vmcnt(15)
	v_lshlrev_b32_e32 v36, 16, v62
	v_and_b32_e32 v34, 0xffff0000, v62
	v_fmac_f32_e32 v36, v142, v46
	v_fmac_f32_e32 v34, v143, v46
	v_cvt_pk_bf16_f32 v34, v36, v34
	v_lshlrev_b32_e32 v36, 16, v63
	v_and_b32_e32 v35, 0xffff0000, v63
	v_fmac_f32_e32 v35, v145, v46
	v_fmac_f32_e32 v36, v144, v46
	v_cvt_pk_bf16_f32 v35, v36, v35
	global_store_dwordx2 v[206:207], v[34:35], off
	s_waitcnt vmcnt(15)
	v_lshlrev_b32_e32 v36, 16, v64
	v_and_b32_e32 v34, 0xffff0000, v64
	v_fmac_f32_e32 v36, v146, v46
	v_fmac_f32_e32 v34, v147, v46
	v_cvt_pk_bf16_f32 v34, v36, v34
	v_lshlrev_b32_e32 v36, 16, v65
	v_and_b32_e32 v35, 0xffff0000, v65
	v_fmac_f32_e32 v35, v149, v46
	v_fmac_f32_e32 v36, v148, v46
	v_cvt_pk_bf16_f32 v35, v36, v35
	global_store_dwordx2 v[206:207], v[34:35], off offset:16
	s_waitcnt vmcnt(15)
	v_lshlrev_b32_e32 v36, 16, v66
	v_and_b32_e32 v34, 0xffff0000, v66
	v_fmac_f32_e32 v36, v150, v46
	v_fmac_f32_e32 v34, v151, v46
	v_cvt_pk_bf16_f32 v34, v36, v34
	v_lshlrev_b32_e32 v36, 16, v67
	v_and_b32_e32 v35, 0xffff0000, v67
	v_fmac_f32_e32 v35, v153, v46
	v_fmac_f32_e32 v36, v152, v46
	v_cvt_pk_bf16_f32 v35, v36, v35
	global_store_dwordx2 v[206:207], v[34:35], off offset:32
	s_waitcnt vmcnt(15)
	v_lshlrev_b32_e32 v36, 16, v68
	v_and_b32_e32 v34, 0xffff0000, v68
	v_fmac_f32_e32 v36, v154, v46
	v_fmac_f32_e32 v34, v155, v46
	v_cvt_pk_bf16_f32 v34, v36, v34
	v_lshlrev_b32_e32 v36, 16, v69
	v_and_b32_e32 v35, 0xffff0000, v69
	v_fmac_f32_e32 v35, v157, v46
	v_fmac_f32_e32 v36, v156, v46
	v_cvt_pk_bf16_f32 v35, v36, v35
	global_store_dwordx2 v[206:207], v[34:35], off offset:48
	s_waitcnt vmcnt(15)
	v_lshlrev_b32_e32 v36, 16, v70
	v_and_b32_e32 v34, 0xffff0000, v70
	v_fmac_f32_e32 v36, v126, v46
	v_fmac_f32_e32 v34, v127, v46
	v_cvt_pk_bf16_f32 v34, v36, v34
	v_lshlrev_b32_e32 v36, 16, v71
	v_and_b32_e32 v35, 0xffff0000, v71
	v_fmac_f32_e32 v35, v129, v46
	v_fmac_f32_e32 v36, v128, v46
	v_cvt_pk_bf16_f32 v35, v36, v35
	global_store_dwordx2 v[206:207], v[34:35], off offset:64
	s_waitcnt vmcnt(15)
	v_lshlrev_b32_e32 v36, 16, v72
	v_and_b32_e32 v34, 0xffff0000, v72
	v_fmac_f32_e32 v36, v130, v46
	v_fmac_f32_e32 v34, v131, v46
	v_cvt_pk_bf16_f32 v34, v36, v34
	v_lshlrev_b32_e32 v36, 16, v73
	v_and_b32_e32 v35, 0xffff0000, v73
	v_fmac_f32_e32 v35, v133, v46
	v_fmac_f32_e32 v36, v132, v46
	v_cvt_pk_bf16_f32 v35, v36, v35
	global_store_dwordx2 v[206:207], v[34:35], off offset:80
	s_waitcnt vmcnt(15)
	v_lshlrev_b32_e32 v36, 16, v74
	v_and_b32_e32 v34, 0xffff0000, v74
	v_fmac_f32_e32 v36, v134, v46
	v_fmac_f32_e32 v34, v135, v46
	v_cvt_pk_bf16_f32 v34, v36, v34
	v_lshlrev_b32_e32 v36, 16, v75
	v_and_b32_e32 v35, 0xffff0000, v75
	v_fmac_f32_e32 v35, v137, v46
	v_fmac_f32_e32 v36, v136, v46
	v_cvt_pk_bf16_f32 v35, v36, v35
	global_store_dwordx2 v[206:207], v[34:35], off offset:96
	s_waitcnt vmcnt(15)
	v_lshlrev_b32_e32 v36, 16, v76
	v_and_b32_e32 v34, 0xffff0000, v76
	v_fmac_f32_e32 v36, v138, v46
	v_fmac_f32_e32 v34, v139, v46
	v_cvt_pk_bf16_f32 v34, v36, v34
	v_lshlrev_b32_e32 v36, 16, v77
	v_and_b32_e32 v35, 0xffff0000, v77
	v_fmac_f32_e32 v35, v141, v46
	v_fmac_f32_e32 v36, v140, v46
	v_cvt_pk_bf16_f32 v35, v36, v35
	global_store_dwordx2 v[206:207], v[34:35], off offset:112
	s_waitcnt vmcnt(15)
	v_lshlrev_b32_e32 v36, 16, v78
	v_and_b32_e32 v34, 0xffff0000, v78
	v_fmac_f32_e32 v36, v110, v46
	v_fmac_f32_e32 v34, v111, v46
	v_cvt_pk_bf16_f32 v34, v36, v34
	v_lshlrev_b32_e32 v36, 16, v79
	v_and_b32_e32 v35, 0xffff0000, v79
	v_fmac_f32_e32 v35, v113, v46
	v_fmac_f32_e32 v36, v112, v46
	v_cvt_pk_bf16_f32 v35, v36, v35
	global_store_dwordx2 v[206:207], v[34:35], off offset:128
	s_waitcnt vmcnt(15)
; #define GAS __attribute__((address_space(1)))
; __device__ __forceinline__ unsigned cvt_pk_bf16(float lo, float hi) { unsigned r; asm volatile("v_cvt_pk_bf16_f32 %0, %1, %2" : "=v"(r) : "v"(lo), "v"(hi)); return r; }
; __device__ __forceinline__ void nsa_unit(const Args& a, LAS unsigned char* lds, int b, int kvh, int qb) {
;     ...
;                     for (int aa = 0; aa < 4; ++aa) { const u32x2 pv = *(const GAS u32x2*)(mp + (32 * dt + 8 * aa) * 2); u32x2 wv;
;                         wv.x = pg8::cvt_pk_bf16(bflo(pv.x) + o[dt][4 * aa] * f, bfhi(pv.x) + o[dt][4 * aa + 1] * f); wv.y = pg8::cvt_pk_bf16(bflo(pv.y) + o[dt][4 * aa + 2] * f, bfhi(pv.y) + o[dt][4 * aa + 3] * f);
;                         *(GAS u32x2*)(mp + (32 * dt + 8 * aa) * 2) = wv; }
; #pragma unroll
;                     for (int i = 0; i < 16; ++i) o[dt][i] = 0.f; }
;                 mrun = -1e30f; lrun = 0.f;
	v_lshlrev_b32_e32 v36, 16, v80
	v_and_b32_e32 v34, 0xffff0000, v80
	v_fmac_f32_e32 v36, v114, v46
	v_fmac_f32_e32 v34, v115, v46
	v_cvt_pk_bf16_f32 v34, v36, v34
	v_lshlrev_b32_e32 v36, 16, v81
	v_and_b32_e32 v35, 0xffff0000, v81
	v_fmac_f32_e32 v35, v117, v46
	v_fmac_f32_e32 v36, v116, v46
	v_cvt_pk_bf16_f32 v35, v36, v35
	global_store_dwordx2 v[206:207], v[34:35], off offset:144
	s_waitcnt vmcnt(15)
	v_lshlrev_b32_e32 v36, 16, v82
	v_and_b32_e32 v34, 0xffff0000, v82
	v_fmac_f32_e32 v36, v118, v46
	v_fmac_f32_e32 v34, v119, v46
	v_cvt_pk_bf16_f32 v34, v36, v34
	v_lshlrev_b32_e32 v36, 16, v83
	v_and_b32_e32 v35, 0xffff0000, v83
	v_fmac_f32_e32 v35, v121, v46
	v_fmac_f32_e32 v36, v120, v46
	v_cvt_pk_bf16_f32 v35, v36, v35
	global_store_dwordx2 v[206:207], v[34:35], off offset:160
	s_waitcnt vmcnt(15)
	v_lshlrev_b32_e32 v36, 16, v84
	v_and_b32_e32 v34, 0xffff0000, v84
	v_fmac_f32_e32 v36, v122, v46
	v_fmac_f32_e32 v34, v123, v46
	v_cvt_pk_bf16_f32 v34, v36, v34
	v_lshlrev_b32_e32 v36, 16, v85
	v_and_b32_e32 v35, 0xffff0000, v85
	v_fmac_f32_e32 v35, v125, v46
	v_fmac_f32_e32 v36, v124, v46
	v_cvt_pk_bf16_f32 v35, v36, v35
	global_store_dwordx2 v[206:207], v[34:35], off offset:176
	s_waitcnt vmcnt(15)
	v_lshlrev_b32_e32 v36, 16, v86
	v_and_b32_e32 v34, 0xffff0000, v86
	v_fmac_f32_e32 v36, v94, v46
	v_fmac_f32_e32 v34, v95, v46
	v_cvt_pk_bf16_f32 v34, v36, v34
	v_lshlrev_b32_e32 v36, 16, v87
	v_and_b32_e32 v35, 0xffff0000, v87
	v_fmac_f32_e32 v35, v97, v46
	v_fmac_f32_e32 v36, v96, v46
	v_cvt_pk_bf16_f32 v35, v36, v35
	global_store_dwordx2 v[206:207], v[34:35], off offset:192
	s_waitcnt vmcnt(15)
	v_lshlrev_b32_e32 v36, 16, v88
	v_and_b32_e32 v34, 0xffff0000, v88
	v_fmac_f32_e32 v36, v98, v46
	v_fmac_f32_e32 v34, v99, v46
	v_cvt_pk_bf16_f32 v34, v36, v34
	v_lshlrev_b32_e32 v36, 16, v89
	v_and_b32_e32 v35, 0xffff0000, v89
	v_fmac_f32_e32 v35, v101, v46
	v_fmac_f32_e32 v36, v100, v46
	v_cvt_pk_bf16_f32 v35, v36, v35
	global_store_dwordx2 v[206:207], v[34:35], off offset:208
	s_waitcnt vmcnt(15)
	v_lshlrev_b32_e32 v36, 16, v90
	v_and_b32_e32 v34, 0xffff0000, v90
	v_fmac_f32_e32 v36, v102, v46
	v_fmac_f32_e32 v34, v103, v46
	v_cvt_pk_bf16_f32 v34, v36, v34
	v_lshlrev_b32_e32 v36, 16, v91
	v_and_b32_e32 v35, 0xffff0000, v91
	v_fmac_f32_e32 v35, v105, v46
	v_fmac_f32_e32 v36, v104, v46
	v_cvt_pk_bf16_f32 v35, v36, v35
	global_store_dwordx2 v[206:207], v[34:35], off offset:224
	s_waitcnt vmcnt(15)
	v_lshlrev_b32_e32 v36, 16, v92
	v_and_b32_e32 v34, 0xffff0000, v92
	v_fmac_f32_e32 v36, v106, v46
	v_fmac_f32_e32 v34, v107, v46
	v_cvt_pk_bf16_f32 v34, v36, v34
	v_lshlrev_b32_e32 v36, 16, v93
	v_and_b32_e32 v35, 0xffff0000, v93
	v_fmac_f32_e32 v35, v109, v46
	v_fmac_f32_e32 v36, v108, v46
	v_cvt_pk_bf16_f32 v35, v36, v35
	global_store_dwordx2 v[206:207], v[34:35], off offset:240
	s_waitcnt vmcnt(0)
	v_mov_b32_e32 v46, v47
	v_mov_b64_e32 v[156:157], v[60:61]
	v_mov_b64_e32 v[140:141], v[60:61]
	v_mov_b64_e32 v[124:125], v[60:61]
	v_mov_b64_e32 v[108:109], v[60:61]
	v_mov_b64_e32 v[154:155], v[58:59]
	v_mov_b64_e32 v[152:153], v[56:57]
	v_mov_b64_e32 v[150:151], v[54:55]
	v_mov_b64_e32 v[148:149], v[52:53]
	v_mov_b64_e32 v[146:147], v[50:51]
	v_mov_b64_e32 v[144:145], v[48:49]
	v_mov_b64_e32 v[142:143], v[46:47]
	v_mov_b64_e32 v[138:139], v[58:59]
	v_mov_b64_e32 v[136:137], v[56:57]
	v_mov_b64_e32 v[134:135], v[54:55]
	v_mov_b64_e32 v[132:133], v[52:53]
	v_mov_b64_e32 v[130:131], v[50:51]
	v_mov_b64_e32 v[128:129], v[48:49]
	v_mov_b64_e32 v[126:127], v[46:47]
	v_mov_b64_e32 v[122:123], v[58:59]
	v_mov_b64_e32 v[120:121], v[56:57]
	v_mov_b64_e32 v[118:119], v[54:55]
	v_mov_b64_e32 v[116:117], v[52:53]
	v_mov_b64_e32 v[114:115], v[50:51]
	v_mov_b64_e32 v[112:113], v[48:49]
	v_mov_b64_e32 v[110:111], v[46:47]
	v_mov_b64_e32 v[106:107], v[58:59]
	v_mov_b64_e32 v[104:105], v[56:57]
	v_mov_b64_e32 v[102:103], v[54:55]
	v_mov_b64_e32 v[100:101], v[52:53]
	v_mov_b64_e32 v[98:99], v[50:51]
	v_mov_b64_e32 v[96:97], v[48:49]
	v_mov_b64_e32 v[94:95], v[46:47]
; #define LAS __attribute__((address_space(3)))
; __device__ __forceinline__ void nsa_dma_tile(const bf16* kt, unsigned kstr, const bf16* vt, unsigned vstr, unsigned ldsK, unsigned ldsV, int w, int lane) {
; #pragma unroll
;     for (int i = 0; i < 2; ++i) { const int q = 2 * w + i, row = 4 * q + (lane >> 4), c = (lane & 15) ^ (row & 15);
;         glds16((const unsigned char*)kt + ((size_t)row * kstr + c * 16), (unsigned)__builtin_amdgcn_readfirstlane((int)(ldsK + q * 1024))); }
; #pragma unroll
;     for (int i = 0; i < 2; ++i) { const int q = 2 * w + i, row = 8 * q + (lane >> 3), c = (lane & 7) ^ ((row >> 1) & 7);
;         glds16((const unsigned char*)vt + ((size_t)row * vstr + c * 16), (unsigned)__builtin_amdgcn_readfirstlane((int)(ldsV + q * 1024))); }
; }
; __device__ __forceinline__ void nsa_qk_sw(const LAS unsigned char* kbuf, const bf16x8 (&qf)[8], int r, int h, f32x16& p0, f32x16& p1) {
;     const int x = r & 15; const LAS unsigned char* kA = kbuf + r * 256 + ((h ^ (x & 1)) * 16); const int xk = (x & 14) * 16;
; #pragma unroll
;     for (int i = 0; i < 16; ++i) { p0[i] = 0.f; p1[i] = 0.f; }
;     bf16x8 a0, a1, b0, b1;
;     a0 = *(const LAS bf16x8*)(kA + (0 ^ xk)); a1 = *(const LAS bf16x8*)(kA + (0 ^ xk) + 8192); __builtin_amdgcn_sched_barrier(0);
; #pragma unroll
;     for (int ks = 0; ks < 8; ks += 2) {
;         b0 = *(const LAS bf16x8*)(kA + (((ks + 1) * 32) ^ xk)); b1 = *(const LAS bf16x8*)(kA + (((ks + 1) * 32) ^ xk) + 8192); __builtin_amdgcn_sched_barrier(0);
;         p0 = __builtin_amdgcn_mfma_f32_32x32x16_bf16(a0, qf[ks], p0, 0, 0, 0); p1 = __builtin_amdgcn_mfma_f32_32x32x16_bf16(a1, qf[ks], p1, 0, 0, 0); __builtin_amdgcn_sched_barrier(0);
;         if (ks + 2 < 8) { a0 = *(const LAS bf16x8*)(kA + (((ks + 2) * 32) ^ xk)); a1 = *(const LAS bf16x8*)(kA + (((ks + 2) * 32) ^ xk) + 8192); } __builtin_amdgcn_sched_barrier(0);
; __device__ __forceinline__ void nsa_unit(const Args& a, LAS unsigned char* lds, int b, int kvh, int qb) {
;     ...
;         asm volatile("s_waitcnt lgkmcnt(0)\n\ts_barrier" ::: "memory");
;         if (it + 2 < nTot) { const bf16 *kt, *vt; tile_src(it + 2, kt, vt); const int t2 = it + 2;
;             int lo_ = lane; asm volatile("" : "+v"(lo_)); nsa_dma_tile(kt, PW * 2, vt, VTP * 2, ldsb + (t2 % 3) * NTB, ldsb + VOFF + (t2 & 3) * NTB, w, lo_); }
.Lpvdone_1:
.LBB0_1858:
	s_waitcnt lgkmcnt(0)
	s_barrier
	s_add_i32 s2, s70, 2
	s_cmp_gt_i32 s2, s17
	s_cbranch_scc1 .LBB0_1860
	s_mul_hi_u32 s3, s68, 0xaaaaaaab
	s_lshr_b32 s3, s3, 1
	s_mul_i32 s3, s3, 0xc000
	s_sub_i32 s33, s20, s3
	s_cmp_gt_i32 s2, s62
	s_cselect_b64 s[2:3], -1, 0
	s_and_b64 s[12:13], s[2:3], exec
	s_cselect_b32 s12, s18, 0
	s_cselect_b32 s15, s89, s87
	s_cselect_b32 s14, s88, s86
	s_add_i32 s12, s12, s70
	s_lshl_b32 s12, s12, 6
	s_addk_i32 s12, 0x80
	s_ashr_i32 s13, s12, 31
	s_mul_i32 vcc_hi, s12, 0x2e00
	s_mul_hi_i32 vcc_lo, s12, 0x2e00
	s_add_u32 s14, s14, vcc_hi
	s_addc_u32 s15, s15, vcc_lo
	s_and_b64 s[2:3], s[2:3], exec
	v_mov_b32_e32 v38, v223
	s_cselect_b32 vcc_lo, s97, s95
	s_cselect_b32 vcc_hi, s96, s94
	s_lshl_b64 s[2:3], s[12:13], 1
	s_add_u32 s2, vcc_hi, s2
	v_ashrrev_i32_e32 v39, 4, v38
	v_add_u32_e32 v36, s63, v39
	s_addc_u32 s3, vcc_lo, s3
	s_add_i32 s12, s71, 0xc000
	v_xor_b32_e32 v34, v36, v38
	s_and_b32 s12, s12, 0xc000
	v_lshlrev_b32_e32 v34, 4, v34
	s_add_i32 s12, s12, 0
	v_and_b32_e32 v46, 0xf0, v34
	v_mov_b64_e32 v[34:35], s[14:15]
	s_add_i32 vcc_lo, s12, 0xc000
	v_mad_i64_i32 v[36:37], s[12:13], v36, s73, v[34:35]
	v_lshl_add_u64 v[36:37], v[36:37], 0, v[46:47]
	s_add_i32 s14, s71, s33
	s_add_i32 s12, s14, 0xc000
	s_mov_b32 s13, m0
	s_mov_b32 m0, s12
	s_nop 0
	global_load_lds_dwordx4 v[36:37], off
	s_mov_b32 m0, s13
	v_add_u32_e32 v36, s21, v39
	v_xor_b32_e32 v37, v36, v38
	v_lshlrev_b32_e32 v37, 4, v37
	v_and_b32_e32 v46, 0xf0, v37
	v_mad_i64_i32 v[34:35], s[12:13], v36, s73, v[34:35]
	v_lshl_add_u64 v[34:35], v[34:35], 0, v[46:47]
	v_ashrrev_i32_e32 v39, 3, v38
	s_add_i32 s12, s14, 0xc400
	s_mov_b32 s13, m0
	s_mov_b32 m0, s12
	s_nop 0
	global_load_lds_dwordx4 v[34:35], off
	s_mov_b32 m0, s13
	v_lshrrev_b32_e32 v34, 1, v39
	v_xor_b32_e32 v34, v34, v38
	v_lshlrev_b32_e32 v34, 4, v34
	v_add_u32_e32 v36, s23, v39
	v_and_b32_e32 v46, 0x70, v34
	v_mov_b64_e32 v[34:35], s[2:3]
	v_mad_i64_i32 v[36:37], s[2:3], v36, s74, v[34:35]
	v_lshl_add_u64 v[36:37], v[36:37], 0, v[46:47]
	s_add_i32 s2, vcc_lo, s19
	s_mov_b32 s3, m0
	s_mov_b32 m0, s2
	s_nop 0
	global_load_lds_dwordx4 v[36:37], off
	s_mov_b32 m0, s3
	v_add_u32_e32 v36, s24, v39
	v_lshrrev_b32_e32 v37, 1, v36
	v_xor_b32_e32 v37, v37, v38
	v_lshlrev_b32_e32 v37, 4, v37
	v_and_b32_e32 v46, 0x70, v37
	v_mad_i64_i32 v[34:35], s[2:3], v36, s74, v[34:35]
	v_lshl_add_u64 v[34:35], v[34:35], 0, v[46:47]
	s_add_i32 s2, vcc_lo, s22
	s_mov_b32 s3, m0
	s_mov_b32 m0, s2
	s_nop 0
	global_load_lds_dwordx4 v[34:35], off
	s_mov_b32 m0, s3
.LBB0_1860:
	v_mov_b32_e32 v210, v222
	v_mov_b32_e32 v211, v45
.LBB0_1863:
	s_cmp_gt_i32 s70, s17
	s_cbranch_scc1 .LBB0_1842
	s_mul_hi_u32 s0, s70, 0xaaaaaaab
	s_lshr_b32 s0, s0, 1
	v_lshlrev_b32_e32 v57, 4, v210
	s_mul_i32 s0, s0, 0xffff4000
	v_lshlrev_b32_e32 v46, 8, v210
	v_bitop3_b32 v34, v210, v211, 1 bitop3:0x6c
	v_and_b32_e32 v58, 0xe0, v57
	s_add_i32 s1, s71, 0
	v_lshlrev_b32_e32 v56, 4, v34
	s_add_i32 s1, s1, s0
	v_or_b32_e32 v220, v46, v58
	v_add3_u32 v220, v220, v56, s1
	ds_read_b128 v[34:37], v220 offset:16384
	ds_read_b128 v[38:41], v220 offset:24576
	v_bitop3_b32 v221, v58, v46, 32 bitop3:0xde
	v_add3_u32 v221, v221, v56, s1
	ds_read_b128 v[48:51], v221 offset:16384
	ds_read_b128 v[52:55], v221 offset:24576
	v_bitop3_b32 v220, v58, v46, 64 bitop3:0xde
	v_add3_u32 v220, v220, v56, s1
	ds_read_b128 v[212:215], v220 offset:16384
	ds_read_b128 v[216:219], v220 offset:24576
	s_waitcnt lgkmcnt(5)
	v_mfma_f32_32x32x16_bf16 v[78:93], v[34:37], v[182:185], 0
	s_waitcnt lgkmcnt(4)
	v_mfma_f32_32x32x16_bf16 v[62:77], v[38:41], v[182:185], 0
	v_bitop3_b32 v221, v58, v46, s60 bitop3:0xde
	v_add3_u32 v221, v221, v56, s1
	ds_read_b128 v[34:37], v221 offset:16384
	ds_read_b128 v[38:41], v221 offset:24576
	s_waitcnt lgkmcnt(5)
	v_mfma_f32_32x32x16_bf16 v[78:93], v[48:51], v[186:189], v[78:93]
	s_waitcnt lgkmcnt(4)
	v_mfma_f32_32x32x16_bf16 v[62:77], v[52:55], v[186:189], v[62:77]
	s_movk_i32 s0, 0x80
	v_bitop3_b32 v220, v58, v46, s0 bitop3:0xde
	v_add3_u32 v220, v220, v56, s1
	ds_read_b128 v[48:51], v220 offset:16384
	ds_read_b128 v[52:55], v220 offset:24576
	s_waitcnt lgkmcnt(5)
	v_mfma_f32_32x32x16_bf16 v[78:93], v[212:215], v[158:161], v[78:93]
	s_waitcnt lgkmcnt(4)
	v_mfma_f32_32x32x16_bf16 v[62:77], v[216:219], v[158:161], v[62:77]
	s_movk_i32 s0, 0xa0
	v_bitop3_b32 v221, v58, v46, s0 bitop3:0xde
	v_add3_u32 v221, v221, v56, s1
	ds_read_b128 v[212:215], v221 offset:16384
	ds_read_b128 v[216:219], v221 offset:24576
	s_waitcnt lgkmcnt(5)
	v_mfma_f32_32x32x16_bf16 v[78:93], v[34:37], v[162:165], v[78:93]
	s_waitcnt lgkmcnt(4)
	v_mfma_f32_32x32x16_bf16 v[62:77], v[38:41], v[162:165], v[62:77]
	s_movk_i32 s0, 0xc0
	v_bitop3_b32 v220, v58, v46, s0 bitop3:0xde
	v_add3_u32 v220, v220, v56, s1
	ds_read_b128 v[34:37], v220 offset:16384
	ds_read_b128 v[38:41], v220 offset:24576
	s_waitcnt lgkmcnt(5)
	v_mfma_f32_32x32x16_bf16 v[78:93], v[48:51], v[166:169], v[78:93]
	s_waitcnt lgkmcnt(4)
	v_mfma_f32_32x32x16_bf16 v[62:77], v[52:55], v[166:169], v[62:77]
	s_movk_i32 s0, 0xe0
	v_bitop3_b32 v221, v57, v46, s0 bitop3:0xce
	v_add3_u32 v221, v221, v56, s1
	ds_read_b128 v[48:51], v221 offset:16384
	ds_read_b128 v[52:55], v221 offset:24576
	s_waitcnt lgkmcnt(5)
	v_mfma_f32_32x32x16_bf16 v[78:93], v[212:215], v[170:173], v[78:93]
	s_waitcnt lgkmcnt(4)
	v_mfma_f32_32x32x16_bf16 v[62:77], v[216:219], v[170:173], v[62:77]
	s_waitcnt lgkmcnt(3)
	v_mfma_f32_32x32x16_bf16 v[78:93], v[34:37], v[174:177], v[78:93]
	s_waitcnt lgkmcnt(2)
	v_mfma_f32_32x32x16_bf16 v[62:77], v[38:41], v[174:177], v[62:77]
	s_waitcnt lgkmcnt(1)
	v_mfma_f32_32x32x16_bf16 v[78:93], v[48:51], v[178:181], v[78:93]
	s_waitcnt lgkmcnt(0)
	v_mfma_f32_32x32x16_bf16 v[62:77], v[52:55], v[178:181], v[62:77]
	s_branch .LBB0_1842
